# GEMM_OUT layer-0 epilogue: the four batch-wide vmcnt(0) replaced by counted waits at each piece's first consumer
# baseline (speedup 1.0000x reference)
.LBB0_1018:
	s_andn2_b64 vcc, exec, s[0:1]
	s_cbranch_vccnz .LBB0_1007
	v_add_u32_e32 v202, 16, v162
	v_ashrrev_i32_e32 v203, 31, v202
	v_lshl_add_u64 v[164:165], v[164:165], 2, s[44:45]
	v_lshlrev_b64 v[166:167], 12, v[162:163]
	v_lshlrev_b64 v[186:187], 12, v[202:203]
	v_lshl_add_u64 v[182:183], v[164:165], 0, v[166:167]
	v_lshl_add_u64 v[198:199], v[164:165], 0, v[186:187]
	global_load_dwordx4 v[166:169], v[182:183], off offset:16
	global_load_dwordx4 v[174:177], v[182:183], off
	global_load_dwordx4 v[178:181], v[182:183], off offset:528
	s_nop 0
	global_load_dwordx4 v[182:185], v[182:183], off offset:512
	s_nop 0
	global_load_dwordx4 v[186:189], v[198:199], off offset:16
	global_load_dwordx4 v[190:193], v[198:199], off
	global_load_dwordx4 v[194:197], v[198:199], off offset:528
	s_nop 0
	global_load_dwordx4 v[198:201], v[198:199], off offset:512
	v_lshlrev_b64 v[204:205], 11, v[162:163]
	s_waitcnt vmcnt(6)
	v_pk_fma_f32 v[130:131], v[130:131], v[146:147], v[176:177]
	v_pk_fma_f32 v[128:129], v[128:129], v[144:145], v[174:175]
	v_pk_fma_f32 v[168:169], v[126:127], v[142:143], v[168:169]
	v_pk_fma_f32 v[126:127], v[124:125], v[140:141], v[166:167]
	v_lshl_add_u64 v[204:205], v[160:161], 0, v[204:205]
	v_cvt_pk_bf16_f32 v124, v128, v129
	v_cvt_pk_bf16_f32 v125, v130, v131
	v_cvt_pk_bf16_f32 v126, v126, v127
	v_cvt_pk_bf16_f32 v127, v168, v169
	global_store_dwordx4 v[204:205], v[124:127], off
	s_waitcnt vmcnt(5)
	v_pk_fma_f32 v[122:123], v[122:123], v[138:139], v[184:185]
	v_pk_fma_f32 v[120:121], v[120:121], v[136:137], v[182:183]
	v_pk_fma_f32 v[124:125], v[114:115], v[134:135], v[180:181]
	v_pk_fma_f32 v[114:115], v[112:113], v[132:133], v[178:179]
	v_cvt_pk_bf16_f32 v112, v120, v121
	v_cvt_pk_bf16_f32 v113, v122, v123
	v_cvt_pk_bf16_f32 v114, v114, v115
	v_cvt_pk_bf16_f32 v115, v124, v125
	global_store_dwordx4 v[204:205], v[112:115], off offset:256
	s_waitcnt vmcnt(4)
	v_pk_fma_f32 v[116:117], v[116:117], v[144:145], v[190:191]
	s_waitcnt vmcnt(2)
	v_pk_fma_f32 v[106:107], v[106:107], v[138:139], v[200:201]
	v_lshlrev_b64 v[112:113], 11, v[202:203]
	v_pk_fma_f32 v[114:115], v[118:119], v[146:147], v[192:193]
	v_pk_fma_f32 v[118:119], v[110:111], v[142:143], v[188:189]
	v_pk_fma_f32 v[110:111], v[108:109], v[140:141], v[186:187]
	v_lshl_add_u64 v[112:113], v[160:161], 0, v[112:113]
	v_cvt_pk_bf16_f32 v108, v116, v117
	v_cvt_pk_bf16_f32 v109, v114, v115
	v_cvt_pk_bf16_f32 v110, v110, v111
	v_cvt_pk_bf16_f32 v111, v118, v119
	global_store_dwordx4 v[112:113], v[108:111], off
	v_pk_fma_f32 v[104:105], v[104:105], v[136:137], v[198:199]
	s_nop 0
	v_pk_fma_f32 v[108:109], v[102:103], v[134:135], v[196:197]
	v_pk_fma_f32 v[102:103], v[100:101], v[132:133], v[194:195]
	v_cvt_pk_bf16_f32 v100, v104, v105
	v_cvt_pk_bf16_f32 v101, v106, v107
	v_cvt_pk_bf16_f32 v102, v102, v103
	v_cvt_pk_bf16_f32 v103, v108, v109
	global_store_dwordx4 v[112:113], v[100:103], off offset:256
	v_add_u32_e32 v166, 32, v162
	v_add_u32_e32 v168, 48, v162
	v_ashrrev_i32_e32 v167, 31, v166
	v_ashrrev_i32_e32 v169, 31, v168
	v_lshlrev_b64 v[100:101], 12, v[166:167]
	v_lshlrev_b64 v[116:117], 12, v[168:169]
	v_lshl_add_u64 v[112:113], v[164:165], 0, v[100:101]
	v_lshl_add_u64 v[128:129], v[164:165], 0, v[116:117]
	global_load_dwordx4 v[100:103], v[112:113], off offset:16
	global_load_dwordx4 v[104:107], v[112:113], off
	global_load_dwordx4 v[108:111], v[112:113], off offset:528
	s_nop 0
	global_load_dwordx4 v[112:115], v[112:113], off offset:512
	s_nop 0
	global_load_dwordx4 v[116:119], v[128:129], off offset:16
	global_load_dwordx4 v[120:123], v[128:129], off
	global_load_dwordx4 v[124:127], v[128:129], off offset:528
	s_nop 0
	global_load_dwordx4 v[128:131], v[128:129], off offset:512
	v_lshlrev_b64 v[166:167], 11, v[166:167]
	s_waitcnt vmcnt(6)
	v_pk_fma_f32 v[98:99], v[98:99], v[146:147], v[106:107]
	v_pk_fma_f32 v[96:97], v[96:97], v[144:145], v[104:105]
	v_pk_fma_f32 v[102:103], v[94:95], v[142:143], v[102:103]
	v_pk_fma_f32 v[94:95], v[92:93], v[140:141], v[100:101]
	v_lshl_add_u64 v[166:167], v[160:161], 0, v[166:167]
	v_cvt_pk_bf16_f32 v92, v96, v97
	v_cvt_pk_bf16_f32 v93, v98, v99
	v_cvt_pk_bf16_f32 v94, v94, v95
	v_cvt_pk_bf16_f32 v95, v102, v103
	global_store_dwordx4 v[166:167], v[92:95], off
	s_waitcnt vmcnt(5)
	v_pk_fma_f32 v[90:91], v[90:91], v[138:139], v[114:115]
	v_pk_fma_f32 v[88:89], v[88:89], v[136:137], v[112:113]
	v_pk_fma_f32 v[92:93], v[82:83], v[134:135], v[110:111]
	v_pk_fma_f32 v[82:83], v[80:81], v[132:133], v[108:109]
	v_cvt_pk_bf16_f32 v80, v88, v89
	v_cvt_pk_bf16_f32 v81, v90, v91
	v_cvt_pk_bf16_f32 v82, v82, v83
	v_cvt_pk_bf16_f32 v83, v92, v93
	global_store_dwordx4 v[166:167], v[80:83], off offset:256
	s_waitcnt vmcnt(4)
	v_pk_fma_f32 v[84:85], v[84:85], v[144:145], v[120:121]
	s_waitcnt vmcnt(2)
	v_pk_fma_f32 v[74:75], v[74:75], v[138:139], v[130:131]
	v_lshlrev_b64 v[80:81], 11, v[168:169]
	v_pk_fma_f32 v[82:83], v[86:87], v[146:147], v[122:123]
	v_pk_fma_f32 v[86:87], v[78:79], v[142:143], v[118:119]
	v_pk_fma_f32 v[78:79], v[76:77], v[140:141], v[116:117]
	v_lshl_add_u64 v[80:81], v[160:161], 0, v[80:81]
	v_cvt_pk_bf16_f32 v76, v84, v85
	v_cvt_pk_bf16_f32 v77, v82, v83
	v_cvt_pk_bf16_f32 v78, v78, v79
	v_cvt_pk_bf16_f32 v79, v86, v87
	global_store_dwordx4 v[80:81], v[76:79], off
	v_pk_fma_f32 v[72:73], v[72:73], v[136:137], v[128:129]
	s_nop 0
	v_pk_fma_f32 v[76:77], v[70:71], v[134:135], v[126:127]
	v_pk_fma_f32 v[70:71], v[68:69], v[132:133], v[124:125]
	v_cvt_pk_bf16_f32 v68, v72, v73
	v_cvt_pk_bf16_f32 v69, v74, v75
	v_cvt_pk_bf16_f32 v70, v70, v71
	v_cvt_pk_bf16_f32 v71, v76, v77
	global_store_dwordx4 v[80:81], v[68:71], off offset:256
	v_add_u32_e32 v100, 0x80, v162
	v_add_u32_e32 v102, 0x90, v162
	v_ashrrev_i32_e32 v101, 31, v100
	v_ashrrev_i32_e32 v103, 31, v102
	v_lshlrev_b64 v[68:69], 12, v[100:101]
	v_lshlrev_b64 v[84:85], 12, v[102:103]
	v_lshl_add_u64 v[80:81], v[164:165], 0, v[68:69]
	v_lshl_add_u64 v[96:97], v[164:165], 0, v[84:85]
	global_load_dwordx4 v[68:71], v[80:81], off offset:16
	global_load_dwordx4 v[72:75], v[80:81], off
	global_load_dwordx4 v[76:79], v[80:81], off offset:528
	s_nop 0
	global_load_dwordx4 v[80:83], v[80:81], off offset:512
	s_nop 0
	global_load_dwordx4 v[84:87], v[96:97], off offset:16
	global_load_dwordx4 v[88:91], v[96:97], off
	global_load_dwordx4 v[92:95], v[96:97], off offset:528
	s_nop 0
	global_load_dwordx4 v[96:99], v[96:97], off offset:512
	v_lshlrev_b64 v[100:101], 11, v[100:101]
	s_waitcnt vmcnt(6)
	v_pk_fma_f32 v[66:67], v[66:67], v[146:147], v[74:75]
	v_pk_fma_f32 v[64:65], v[64:65], v[144:145], v[72:73]
	v_pk_fma_f32 v[70:71], v[62:63], v[142:143], v[70:71]
	v_pk_fma_f32 v[62:63], v[60:61], v[140:141], v[68:69]
	v_lshl_add_u64 v[100:101], v[160:161], 0, v[100:101]
	v_cvt_pk_bf16_f32 v60, v64, v65
	v_cvt_pk_bf16_f32 v61, v66, v67
	v_cvt_pk_bf16_f32 v62, v62, v63
	v_cvt_pk_bf16_f32 v63, v70, v71
	global_store_dwordx4 v[100:101], v[60:63], off
	s_waitcnt vmcnt(5)
	v_pk_fma_f32 v[54:55], v[54:55], v[138:139], v[82:83]
	v_pk_fma_f32 v[52:53], v[52:53], v[136:137], v[80:81]
	v_pk_fma_f32 v[60:61], v[46:47], v[134:135], v[78:79]
	v_pk_fma_f32 v[46:47], v[44:45], v[132:133], v[76:77]
	v_cvt_pk_bf16_f32 v44, v52, v53
	v_cvt_pk_bf16_f32 v45, v54, v55
	v_cvt_pk_bf16_f32 v46, v46, v47
	v_cvt_pk_bf16_f32 v47, v60, v61
	global_store_dwordx4 v[100:101], v[44:47], off offset:256
	s_waitcnt vmcnt(5)
	v_pk_fma_f32 v[50:51], v[50:51], v[142:143], v[86:87]
	v_pk_fma_f32 v[48:49], v[48:49], v[140:141], v[84:85]
	v_lshlrev_b64 v[44:45], 11, v[102:103]
	v_lshl_add_u64 v[52:53], v[160:161], 0, v[44:45]
	s_waitcnt vmcnt(4)
	v_pk_fma_f32 v[46:47], v[58:59], v[146:147], v[90:91]
	v_pk_fma_f32 v[44:45], v[56:57], v[144:145], v[88:89]
	s_waitcnt vmcnt(2)
	v_pk_fma_f32 v[42:43], v[42:43], v[138:139], v[98:99]
	v_cvt_pk_bf16_f32 v44, v44, v45
	v_cvt_pk_bf16_f32 v45, v46, v47
	v_cvt_pk_bf16_f32 v46, v48, v49
	v_cvt_pk_bf16_f32 v47, v50, v51
	global_store_dwordx4 v[52:53], v[44:47], off
	v_pk_fma_f32 v[40:41], v[40:41], v[136:137], v[96:97]
	s_nop 0
	v_pk_fma_f32 v[44:45], v[38:39], v[134:135], v[94:95]
	v_pk_fma_f32 v[38:39], v[36:37], v[132:133], v[92:93]
	v_cvt_pk_bf16_f32 v36, v40, v41
	v_cvt_pk_bf16_f32 v37, v42, v43
	v_cvt_pk_bf16_f32 v38, v38, v39
	v_cvt_pk_bf16_f32 v39, v44, v45
	global_store_dwordx4 v[52:53], v[36:39], off offset:256
	v_add_u32_e32 v68, 0xa0, v162
	v_add_u32_e32 v70, 0xb0, v162
	v_ashrrev_i32_e32 v69, 31, v68
	v_ashrrev_i32_e32 v71, 31, v70
	v_lshlrev_b64 v[36:37], 12, v[68:69]
	v_lshlrev_b64 v[52:53], 12, v[70:71]
	v_lshl_add_u64 v[48:49], v[164:165], 0, v[36:37]
	v_lshl_add_u64 v[64:65], v[164:165], 0, v[52:53]
	global_load_dwordx4 v[36:39], v[48:49], off offset:16
	global_load_dwordx4 v[40:43], v[48:49], off
	global_load_dwordx4 v[44:47], v[48:49], off offset:528
	s_nop 0
	global_load_dwordx4 v[48:51], v[48:49], off offset:512
	s_nop 0
	global_load_dwordx4 v[52:55], v[64:65], off offset:16
	global_load_dwordx4 v[56:59], v[64:65], off
	global_load_dwordx4 v[60:63], v[64:65], off offset:528
	s_nop 0
	global_load_dwordx4 v[64:67], v[64:65], off offset:512
	v_lshlrev_b64 v[68:69], 11, v[68:69]
	s_waitcnt vmcnt(6)
	v_pk_fma_f32 v[32:33], v[32:33], v[146:147], v[42:43]
	v_pk_fma_f32 v[30:31], v[30:31], v[144:145], v[40:41]
	v_pk_fma_f32 v[38:39], v[28:29], v[142:143], v[38:39]
	v_pk_fma_f32 v[28:29], v[26:27], v[140:141], v[36:37]
	v_lshl_add_u64 v[68:69], v[160:161], 0, v[68:69]
	v_cvt_pk_bf16_f32 v26, v30, v31
	v_cvt_pk_bf16_f32 v27, v32, v33
	v_cvt_pk_bf16_f32 v28, v28, v29
	v_cvt_pk_bf16_f32 v29, v38, v39
	global_store_dwordx4 v[68:69], v[26:29], off
	s_waitcnt vmcnt(5)
	v_pk_fma_f32 v[20:21], v[20:21], v[138:139], v[50:51]
	v_pk_fma_f32 v[18:19], v[18:19], v[136:137], v[48:49]
	v_pk_fma_f32 v[26:27], v[12:13], v[134:135], v[46:47]
	v_pk_fma_f32 v[12:13], v[10:11], v[132:133], v[44:45]
	v_cvt_pk_bf16_f32 v10, v18, v19
	v_cvt_pk_bf16_f32 v11, v20, v21
	v_cvt_pk_bf16_f32 v12, v12, v13
	v_cvt_pk_bf16_f32 v13, v26, v27
	global_store_dwordx4 v[68:69], v[10:13], off offset:256
	s_waitcnt vmcnt(5)
	v_pk_fma_f32 v[16:17], v[16:17], v[142:143], v[54:55]
	v_pk_fma_f32 v[14:15], v[14:15], v[140:141], v[52:53]
	v_lshlrev_b64 v[10:11], 11, v[70:71]
	v_lshl_add_u64 v[18:19], v[160:161], 0, v[10:11]
	s_waitcnt vmcnt(4)
	v_pk_fma_f32 v[12:13], v[24:25], v[146:147], v[58:59]
	v_pk_fma_f32 v[10:11], v[22:23], v[144:145], v[56:57]
	s_waitcnt vmcnt(2)
	v_pk_fma_f32 v[8:9], v[8:9], v[138:139], v[66:67]
	v_cvt_pk_bf16_f32 v10, v10, v11
	v_cvt_pk_bf16_f32 v11, v12, v13
	v_cvt_pk_bf16_f32 v12, v14, v15
	v_cvt_pk_bf16_f32 v13, v16, v17
	global_store_dwordx4 v[18:19], v[10:13], off
	v_pk_fma_f32 v[6:7], v[6:7], v[136:137], v[64:65]
	s_nop 0
	v_pk_fma_f32 v[10:11], v[4:5], v[134:135], v[62:63]
	v_pk_fma_f32 v[4:5], v[2:3], v[132:133], v[60:61]
	v_cvt_pk_bf16_f32 v2, v6, v7
	v_cvt_pk_bf16_f32 v3, v8, v9
	v_cvt_pk_bf16_f32 v4, v4, v5
	v_cvt_pk_bf16_f32 v5, v10, v11
	global_store_dwordx4 v[18:19], v[2:5], off offset:256
	s_branch .LBB0_1007
